# speedup vs baseline: 1.0310x; 1.0310x over previous
.LBB2_12:
	v_max3_f32 v69, v46, v47, v48
	s_and_b64 vcc, exec, s[38:39]
	s_nop 1
	v_max3_f32 v69, v69, v49, v42
	v_max3_f32 v69, v69, v43, v44
	v_max3_f32 v69, v69, v45, v38
	v_max3_f32 v69, v69, v39, v40
	v_max3_f32 v69, v69, v41, v34
	v_max3_f32 v69, v69, v35, v36
	v_max_f32_e32 v69, v69, v37
	s_cbranch_vccnz .Lattn_first_tile
	v_cmp_lt_f32_e32 vcc, s58, v69
	s_nop 1
	s_cbranch_vccz .LBB2_5
	v_mov_b32_e32 v71, v69
	s_nop 1
	v_permlane16_swap_b32_e32 v69, v71
	v_max_f32_e32 v69, v69, v71
	v_mov_b32_e32 v71, v69
	s_nop 1
	v_permlane32_swap_b32_e32 v69, v71
	v_max_f32_e32 v69, v69, v71
	v_max_f32_e32 v71, v69, v69
	v_max_f32_e32 v80, 0, v71
	s_branch .Lattn_rescale
.Lattn_first_tile:
	v_mov_b32_e32 v71, v69
	s_nop 1
	v_permlane16_swap_b32_e32 v69, v71
	v_max_f32_e32 v69, v69, v71
	v_mov_b32_e32 v71, v69
	s_nop 1
	v_permlane32_swap_b32_e32 v69, v71
	v_max_f32_e32 v69, v69, v71
	v_mov_b32_e32 v80, v69
